# speedup vs baseline: 1.0125x; 1.0125x over previous
.LBB1_8:
	s_or_b64 exec, exec, s[4:5]
	s_waitcnt vmcnt(1)
	v_mov_b32_e32 v184, 1
	v_lshl_add_u32 v180, v176, 2, v172
	v_lshl_add_u32 v181, v177, 2, v172
	v_lshl_add_u32 v182, v178, 2, v172
	v_lshl_add_u32 v183, v179, 2, v172
	s_waitcnt lgkmcnt(0)
	ds_add_u32 v180, v184
	ds_add_u32 v181, v184
	ds_add_u32 v182, v184
	ds_add_u32 v183, v184
	s_waitcnt lgkmcnt(0)
	ds_read_b32 v151, v173
	s_waitcnt lgkmcnt(0)
	v_cvt_f32_i32_e32 v185, v151
	ds_write_b32 v173, v185 offset:256
	v_add_u32_e32 v10, v172, v2
	s_waitcnt vmcnt(1) lgkmcnt(0)
	s_barrier
	s_nop 0
	ds_read_b128 v[18:21], v10 offset:256
	ds_read_b128 v[22:25], v10 offset:288
	ds_read_b128 v[82:85], v10 offset:320
	ds_read_b128 v[86:89], v10 offset:352
	ds_read_b128 v[74:77], v10 offset:384
	ds_read_b128 v[78:81], v10 offset:416
	ds_read_b128 v[2:5], v213 offset:32768
	ds_read_b128 v[6:9], v213 offset:0
	ds_read_b128 v[66:69], v10 offset:448
	ds_read_b128 v[70:73], v10 offset:480
	ds_read_b128 v[10:13], v213 offset:1024
	s_waitcnt lgkmcnt(3)
	v_pk_mul_f32 v[26:27], v[8:9], v[20:21]
	v_pk_mul_f32 v[28:29], v[6:7], v[18:19]
	ds_read_b128 v[14:17], v213 offset:8192
	s_waitcnt lgkmcnt(1)
	v_pk_mul_f32 v[12:13], v[12:13], v[24:25]
	v_pk_mul_f32 v[10:11], v[10:11], v[22:23]
	v_pk_fma_f32 v[30:31], v[8:9], v[20:21], v[12:13]
	v_pk_fma_f32 v[32:33], v[6:7], v[18:19], v[10:11]
	v_cvt_pk_bf16_f32 v9, v12, v13
	v_cvt_pk_bf16_f32 v7, v26, v27
	v_cvt_pk_bf16_f32 v8, v10, v11
	v_cvt_pk_bf16_f32 v6, v28, v29
	ds_read_b128 v[10:13], v213 offset:33792
	s_nop 0
	v_mfma_f32_32x32x16_bf16 v[34:49], v[2:5], v[6:9], 0
	ds_read_b128 v[6:9], v213 offset:9216
	s_waitcnt lgkmcnt(2)
	v_mul_f32_e32 v26, v16, v20
	v_mul_f32_e32 v27, v17, v21
	v_pk_mul_f32 v[50:51], v[14:15], v[18:19]
	s_mov_b32 s4, 0x3727c5ac
	s_waitcnt lgkmcnt(0)
	v_pk_mul_f32 v[8:9], v[8:9], v[24:25]
	v_pk_mul_f32 v[28:29], v[6:7], v[22:23]
	v_pk_fma_f32 v[90:91], v[16:17], v[20:21], v[8:9]
	v_pk_fma_f32 v[92:93], v[14:15], v[18:19], v[28:29]
	ds_read_b128 v[14:17], v213 offset:2048
	v_cvt_pk_bf16_f32 v9, v8, v9
	v_cvt_pk_bf16_f32 v7, v26, v27
	v_cvt_pk_bf16_f32 v8, v28, v29
	ds_read_b128 v[26:29], v213 offset:3072
	v_cvt_pk_bf16_f32 v6, v50, v51
	s_waitcnt lgkmcnt(1)
	v_pk_mul_f32 v[94:95], v[14:15], v[82:83]
	s_mov_b32 s0, 0x3c800000
	v_mfma_f32_32x32x16_bf16 v[50:65], v[2:5], v[6:9], 0
	v_mul_f32_e32 v2, v16, v84
	v_mul_f32_e32 v3, v17, v85
	s_waitcnt lgkmcnt(0)
	v_mul_f32_e32 v4, v28, v88
	v_mul_f32_e32 v5, v29, v89
	v_pk_mul_f32 v[6:7], v[26:27], v[86:87]
	v_pk_fma_f32 v[8:9], v[16:17], v[84:85], v[4:5]
	v_cvt_pk_bf16_f32 v3, v2, v3
	v_pk_fma_f32 v[14:15], v[14:15], v[82:83], v[6:7]
	v_pk_add_f32 v[26:27], v[8:9], v[30:31]
	v_cvt_pk_bf16_f32 v5, v4, v5
	v_cvt_pk_bf16_f32 v4, v6, v7
	ds_read_b128 v[6:9], v213 offset:10240
	v_pk_add_f32 v[28:29], v[14:15], v[32:33]
	ds_read_b128 v[14:17], v213 offset:11264
	v_cvt_pk_bf16_f32 v2, v94, v95
	s_waitcnt lgkmcnt(1)
	v_pk_mul_f32 v[30:31], v[6:7], v[82:83]
	v_mov_b64_e32 v[152:153], s[4:5]
	v_mfma_f32_32x32x16_bf16 v[34:49], v[10:13], v[2:5], v[34:49]
	v_mul_f32_e32 v2, v8, v84
	v_mul_f32_e32 v3, v9, v85
	s_waitcnt lgkmcnt(0)
	v_mul_f32_e32 v4, v16, v88
	v_mul_f32_e32 v5, v17, v89
	v_pk_mul_f32 v[14:15], v[14:15], v[86:87]
	v_pk_fma_f32 v[8:9], v[8:9], v[84:85], v[4:5]
	v_pk_fma_f32 v[6:7], v[6:7], v[82:83], v[14:15]
	v_cvt_pk_bf16_f32 v5, v4, v5
	v_cvt_pk_bf16_f32 v3, v2, v3
	v_cvt_pk_bf16_f32 v4, v14, v15
	v_pk_add_f32 v[32:33], v[8:9], v[90:91]
	v_pk_add_f32 v[90:91], v[6:7], v[92:93]
	ds_read_b128 v[6:9], v213 offset:34816
	ds_read_b128 v[14:17], v213 offset:4096
	v_cvt_pk_bf16_f32 v2, v30, v31
	s_mov_b32 s13, 0
	s_mov_b64 s[6:7], 0
	v_mfma_f32_32x32x16_bf16 v[50:65], v[10:13], v[2:5], v[50:65]
	ds_read_b128 v[2:5], v213 offset:5120
	ds_read_b128 v[10:13], v213 offset:12288
	s_waitcnt lgkmcnt(2)
	v_pk_mul_f32 v[30:31], v[16:17], v[76:77]
	v_pk_mul_f32 v[92:93], v[14:15], v[74:75]
	s_waitcnt lgkmcnt(1)
	v_pk_mul_f32 v[4:5], v[4:5], v[80:81]
	v_pk_mul_f32 v[94:95], v[2:3], v[78:79]
	v_pk_fma_f32 v[2:3], v[16:17], v[76:77], v[4:5]
	v_cvt_pk_bf16_f32 v5, v4, v5
	v_pk_add_f32 v[96:97], v[2:3], v[26:27]
	v_cvt_pk_bf16_f32 v3, v30, v31
	v_cvt_pk_bf16_f32 v4, v94, v95
	v_cvt_pk_bf16_f32 v2, v92, v93
	v_pk_fma_f32 v[14:15], v[14:15], v[74:75], v[94:95]
	s_waitcnt lgkmcnt(0)
	v_pk_mul_f32 v[30:31], v[10:11], v[74:75]
	v_mfma_f32_32x32x16_bf16 v[34:49], v[6:9], v[2:5], v[34:49]
	ds_read_b128 v[2:5], v213 offset:13312
	v_add_f32_e32 v98, v14, v28
	v_add_f32_e32 v99, v15, v29
	ds_read_b128 v[14:17], v213 offset:35840
	v_pk_mul_f32 v[26:27], v[12:13], v[76:77]
	s_waitcnt lgkmcnt(1)
	v_pk_mul_f32 v[4:5], v[4:5], v[80:81]
	v_pk_mul_f32 v[28:29], v[2:3], v[78:79]
	v_pk_fma_f32 v[2:3], v[12:13], v[76:77], v[4:5]
	v_pk_fma_f32 v[10:11], v[10:11], v[74:75], v[28:29]
	v_pk_add_f32 v[32:33], v[2:3], v[32:33]
	v_pk_add_f32 v[92:93], v[10:11], v[90:91]
	ds_read_b128 v[10:13], v213 offset:6144
	v_cvt_pk_bf16_f32 v5, v4, v5
	v_cvt_pk_bf16_f32 v3, v26, v27
	v_cvt_pk_bf16_f32 v4, v28, v29
	ds_read_b128 v[26:29], v213 offset:7168
	v_cvt_pk_bf16_f32 v2, v30, v31
	s_waitcnt lgkmcnt(1)
	v_pk_mul_f32 v[30:31], v[10:11], v[66:67]
	v_mfma_f32_32x32x16_bf16 v[50:65], v[6:9], v[2:5], v[50:65]
	v_mul_f32_e32 v2, v12, v68
	v_mul_f32_e32 v3, v13, v69
	s_waitcnt lgkmcnt(0)
	v_mul_f32_e32 v4, v28, v72
	v_mul_f32_e32 v5, v29, v73
	v_pk_mul_f32 v[6:7], v[26:27], v[70:71]
	v_pk_fma_f32 v[8:9], v[12:13], v[68:69], v[4:5]
	v_cvt_pk_bf16_f32 v3, v2, v3
	v_pk_fma_f32 v[10:11], v[10:11], v[66:67], v[6:7]
	v_pk_add_f32 v[94:95], v[8:9], v[96:97]
	v_cvt_pk_bf16_f32 v5, v4, v5
	v_cvt_pk_bf16_f32 v4, v6, v7
	ds_read_b128 v[6:9], v213 offset:14336
	v_pk_add_f32 v[96:97], v[10:11], v[98:99]
	ds_read_b128 v[10:13], v213 offset:15360
	v_cvt_pk_bf16_f32 v2, v30, v31
	s_waitcnt lgkmcnt(1)
	v_pk_mul_f32 v[30:31], v[6:7], v[66:67]
	v_mfma_f32_32x32x16_bf16 v[34:49], v[14:17], v[2:5], v[34:49]
	s_waitcnt lgkmcnt(0)
	v_mul_f32_e32 v10, v10, v70
	v_mul_f32_e32 v11, v11, v71
	v_mul_f32_e32 v2, v8, v68
	v_mul_f32_e32 v3, v9, v69
	v_pk_mul_f32 v[4:5], v[12:13], v[72:73]
	v_pk_fma_f32 v[6:7], v[6:7], v[66:67], v[10:11]
	v_pk_fma_f32 v[8:9], v[8:9], v[68:69], v[4:5]
	v_pk_add_f32 v[92:93], v[6:7], v[92:93]
	v_cvt_pk_bf16_f32 v3, v2, v3
	v_pk_add_f32 v[90:91], v[8:9], v[32:33]
	v_cvt_pk_bf16_f32 v5, v4, v5
	v_cvt_pk_bf16_f32 v4, v10, v11
	ds_read_b128 v[26:29], v213 offset:36864
	ds_read_b128 v[6:9], v213 offset:16384
	v_cvt_pk_bf16_f32 v2, v30, v31
	ds_read_b128 v[98:101], v213 offset:25600
	ds_read_b128 v[102:105], v213 offset:37888
	v_mfma_f32_32x32x16_bf16 v[50:65], v[14:17], v[2:5], v[50:65]
	ds_read_b128 v[2:5], v213 offset:17408
	ds_read_b128 v[30:33], v213 offset:24576
	s_waitcnt lgkmcnt(4)
	v_pk_mul_f32 v[12:13], v[6:7], v[18:19]
	v_pk_mul_f32 v[10:11], v[8:9], v[20:21]
	s_waitcnt lgkmcnt(1)
	v_pk_mul_f32 v[14:15], v[2:3], v[22:23]
	v_pk_mul_f32 v[22:23], v[98:99], v[22:23]
	v_pk_fma_f32 v[112:113], v[6:7], v[18:19], v[14:15]
	s_waitcnt lgkmcnt(0)
	v_pk_mul_f32 v[114:115], v[30:31], v[18:19]
	v_pk_fma_f32 v[118:119], v[30:31], v[18:19], v[22:23]
	v_pk_mul_f32 v[4:5], v[4:5], v[24:25]
	v_pk_mul_f32 v[106:107], v[32:33], v[20:21]
	v_pk_mul_f32 v[24:25], v[100:101], v[24:25]
	ds_read_b128 v[98:101], v213 offset:18432
	v_cvt_pk_bf16_f32 v19, v106, v107
	ds_read_b128 v[106:109], v213 offset:19456
	v_pk_fma_f32 v[110:111], v[8:9], v[20:21], v[4:5]
	v_cvt_pk_bf16_f32 v5, v4, v5
	v_cvt_pk_bf16_f32 v3, v10, v11
	v_cvt_pk_bf16_f32 v4, v14, v15
	s_waitcnt lgkmcnt(0)
	v_pk_mul_f32 v[106:107], v[106:107], v[86:87]
	v_cvt_pk_bf16_f32 v2, v12, v13
	v_pk_mul_f32 v[120:121], v[98:99], v[82:83]
	v_pk_mul_f32 v[108:109], v[108:109], v[88:89]
	v_pk_fma_f32 v[98:99], v[98:99], v[82:83], v[106:107]
	v_mfma_f32_32x32x16_bf16 v[2:17], v[26:29], v[2:5], 0
	v_cvt_pk_bf16_f32 v18, v114, v115
	v_mul_f32_e32 v114, v100, v84
	v_mul_f32_e32 v115, v101, v85
	v_fma_f32 v100, v100, v84, v108
	v_fma_f32 v101, v101, v85, v109
	v_pk_add_f32 v[124:125], v[98:99], v[112:113]
	v_pk_add_f32 v[122:123], v[100:101], v[110:111]
	v_cvt_pk_bf16_f32 v101, v108, v109
	v_cvt_pk_bf16_f32 v100, v106, v107
	ds_read_b128 v[106:109], v213 offset:26624
	v_pk_fma_f32 v[116:117], v[32:33], v[20:21], v[24:25]
	v_cvt_pk_bf16_f32 v21, v24, v25
	v_cvt_pk_bf16_f32 v20, v22, v23
	ds_read_b128 v[110:113], v213 offset:27648
	v_cvt_pk_bf16_f32 v99, v114, v115
	v_mfma_f32_32x32x16_bf16 v[18:33], v[26:29], v[18:21], 0
	v_cvt_pk_bf16_f32 v98, v120, v121
	s_waitcnt lgkmcnt(1)
	v_mul_f32_e32 v114, v106, v82
	v_mul_f32_e32 v115, v107, v83
	s_waitcnt lgkmcnt(0)
	v_pk_mul_f32 v[86:87], v[110:111], v[86:87]
	v_pk_mul_f32 v[88:89], v[112:113], v[88:89]
	v_pk_fma_f32 v[82:83], v[106:107], v[82:83], v[86:87]
	v_mfma_f32_32x32x16_bf16 v[2:17], v[102:105], v[98:101], v[2:17]
	v_mul_f32_e32 v98, v108, v84
	v_mul_f32_e32 v99, v109, v85
	v_fma_f32 v84, v108, v84, v88
	v_fma_f32 v85, v109, v85, v89
	v_add_f32_e32 v108, v82, v118
	v_add_f32_e32 v109, v83, v119
	v_cvt_pk_bf16_f32 v83, v98, v99
	v_pk_add_f32 v[106:107], v[84:85], v[116:117]
	v_cvt_pk_bf16_f32 v85, v88, v89
	v_cvt_pk_bf16_f32 v84, v86, v87
	ds_read_b128 v[86:89], v213 offset:38912
	ds_read_b128 v[98:101], v213 offset:20480
	v_cvt_pk_bf16_f32 v82, v114, v115
	s_waitcnt lgkmcnt(0)
	v_pk_mul_f32 v[110:111], v[100:101], v[76:77]
	v_mfma_f32_32x32x16_bf16 v[18:33], v[102:105], v[82:85], v[18:33]
	ds_read_b128 v[82:85], v213 offset:21504
	ds_read_b128 v[102:105], v213 offset:28672
	v_mul_f32_e32 v112, v98, v74
	v_mul_f32_e32 v113, v99, v75
	s_waitcnt lgkmcnt(1)
	v_pk_mul_f32 v[84:85], v[84:85], v[80:81]
	v_pk_mul_f32 v[114:115], v[82:83], v[78:79]
	v_pk_fma_f32 v[82:83], v[100:101], v[76:77], v[84:85]
	v_cvt_pk_bf16_f32 v85, v84, v85
	v_pk_add_f32 v[116:117], v[82:83], v[122:123]
	v_cvt_pk_bf16_f32 v83, v110, v111
	v_cvt_pk_bf16_f32 v84, v114, v115
	v_cvt_pk_bf16_f32 v82, v112, v113
	v_pk_fma_f32 v[98:99], v[98:99], v[74:75], v[114:115]
	s_waitcnt lgkmcnt(0)
	v_pk_mul_f32 v[112:113], v[102:103], v[74:75]
	v_mfma_f32_32x32x16_bf16 v[2:17], v[86:89], v[82:85], v[2:17]
	ds_read_b128 v[82:85], v213 offset:29696
	v_add_f32_e32 v118, v98, v124
	v_add_f32_e32 v119, v99, v125
	v_mul_f32_e32 v110, v104, v76
	v_mul_f32_e32 v111, v105, v77
	ds_read_b128 v[98:101], v213 offset:39936
	s_waitcnt lgkmcnt(1)
	v_pk_mul_f32 v[78:79], v[82:83], v[78:79]
	v_pk_mul_f32 v[80:81], v[84:85], v[80:81]
	v_pk_fma_f32 v[74:75], v[102:103], v[74:75], v[78:79]
	v_pk_fma_f32 v[76:77], v[104:105], v[76:77], v[80:81]
	v_pk_add_f32 v[104:105], v[74:75], v[108:109]
	v_pk_add_f32 v[102:103], v[76:77], v[106:107]
	v_cvt_pk_bf16_f32 v77, v80, v81
	v_cvt_pk_bf16_f32 v76, v78, v79
	ds_read_b128 v[78:81], v213 offset:22528
	ds_read_b128 v[82:85], v213 offset:23552
	v_cvt_pk_bf16_f32 v75, v110, v111
	v_cvt_pk_bf16_f32 v74, v112, v113
	s_waitcnt lgkmcnt(0)
	v_pk_mul_f32 v[82:83], v[82:83], v[70:71]
	v_mfma_f32_32x32x16_bf16 v[18:33], v[86:89], v[74:77], v[18:33]
	v_mul_f32_e32 v74, v80, v68
	v_mul_f32_e32 v75, v81, v69
	v_mul_f32_e32 v76, v84, v72
	v_mul_f32_e32 v77, v85, v73
	v_mul_f32_e32 v86, v78, v66
	v_mul_f32_e32 v87, v79, v67
	v_pk_fma_f32 v[80:81], v[80:81], v[68:69], v[76:77]
	v_pk_fma_f32 v[78:79], v[78:79], v[66:67], v[82:83]
	v_cvt_pk_bf16_f32 v75, v74, v75
	v_pk_add_f32 v[88:89], v[80:81], v[116:117]
	v_pk_add_f32 v[106:107], v[78:79], v[118:119]
	ds_read_b128 v[78:81], v213 offset:30720
	v_cvt_pk_bf16_f32 v77, v76, v77
	v_cvt_pk_bf16_f32 v76, v82, v83
	ds_read_b128 v[82:85], v213 offset:31744
	v_cvt_pk_bf16_f32 v74, v86, v87
	s_waitcnt lgkmcnt(0)
	v_pk_mul_f32 v[72:73], v[84:85], v[72:73]
	v_mfma_f32_32x32x16_bf16 v[2:17], v[98:101], v[74:77], v[2:17]
	v_mul_f32_e32 v74, v80, v68
	v_mul_f32_e32 v75, v81, v69
	v_fma_f32 v68, v80, v68, v72
	v_fma_f32 v69, v81, v69, v73
	v_mul_f32_e32 v70, v82, v70
	v_mul_f32_e32 v71, v83, v71
	v_pk_add_f32 v[84:85], v[68:69], v[102:103]
	v_cvt_pk_bf16_f32 v69, v72, v73
	v_pk_mov_b32 v[72:73], v[96:97], v[94:95] op_sel:[1,0]
	v_mov_b32_e32 v97, v95
	v_pk_add_f32 v[72:73], v[72:73], v[96:97]
	v_pk_mul_f32 v[76:77], v[78:79], v[66:67]
	v_pk_fma_f32 v[66:67], v[78:79], v[66:67], v[70:71]
	v_pk_add_f32 v[72:73], v[72:73], v[72:73] op_sel:[0,1] op_sel_hi:[1,0]
	v_pk_add_f32 v[86:87], v[66:67], v[104:105]
	v_mov_b32_e32 v66, v72
	s_nop 1
	v_permlane32_swap_b32_e32 v72, v66
	v_add_f32_e32 v66, v72, v66
	v_cvt_pk_bf16_f32 v67, v74, v75
	v_rcp_f32_e32 v74, v66
	v_cvt_pk_bf16_f32 v68, v70, v71
	v_cvt_pk_bf16_f32 v66, v76, v77
	v_pk_mul_f32 v[70:71], v[46:47], v[74:75] op_sel_hi:[1,0]
	s_nop 0
	v_mfma_f32_32x32x16_bf16 v[18:33], v[98:101], v[66:69], v[18:33]
	v_mul_f32_e32 v66, v42, v74
	v_mul_f32_e32 v67, v43, v74
	v_pk_mov_b32 v[42:43], v[92:93], v[90:91] op_sel:[1,0]
	v_mov_b32_e32 v93, v91
	v_pk_add_f32 v[42:43], v[42:43], v[92:93]
	v_pk_mul_f32 v[68:69], v[44:45], v[74:75] op_sel_hi:[1,0]
	v_pk_add_f32 v[42:43], v[42:43], v[42:43] op_sel:[0,1] op_sel_hi:[1,0]
	v_pk_mov_b32 v[44:45], v[106:107], v[88:89] op_sel:[1,0]
	v_mov_b32_e32 v43, v42
	s_nop 1
	v_permlane32_swap_b32_e32 v42, v43
	v_add_f32_e32 v42, v42, v43
	v_rcp_f32_e32 v42, v42
	v_mov_b32_e32 v107, v89
	v_pk_add_f32 v[44:45], v[44:45], v[106:107]
	v_pk_mul_f32 v[72:73], v[48:49], v[74:75] op_sel_hi:[1,0]
	v_pk_add_f32 v[44:45], v[44:45], v[44:45] op_sel:[0,1] op_sel_hi:[1,0]
	v_pk_mul_f32 v[36:37], v[36:37], v[74:75] op_sel_hi:[1,0]
	v_pk_mul_f32 v[38:39], v[38:39], v[74:75] op_sel_hi:[1,0]
	v_pk_mul_f32 v[40:41], v[40:41], v[74:75] op_sel_hi:[1,0]
	v_pk_mul_f32 v[34:35], v[34:35], v[74:75] op_sel_hi:[1,0]
	v_pk_mul_f32 v[74:75], v[58:59], v[42:43] op_sel_hi:[1,0]
	v_pk_mul_f32 v[78:79], v[60:61], v[42:43] op_sel_hi:[1,0]
	v_pk_mul_f32 v[80:81], v[62:63], v[42:43] op_sel_hi:[1,0]
	v_pk_mul_f32 v[82:83], v[64:65], v[42:43] op_sel_hi:[1,0]
	v_pk_mul_f32 v[92:93], v[52:53], v[42:43] op_sel_hi:[1,0]
	v_mov_b32_e32 v43, v44
	s_nop 1
	v_permlane32_swap_b32_e32 v44, v43
	v_add_f32_e32 v43, v44, v43
	v_rcp_f32_e32 v76, v43
	v_pk_mul_f32 v[96:97], v[54:55], v[42:43] op_sel_hi:[1,0]
	v_pk_mul_f32 v[94:95], v[56:57], v[42:43] op_sel_hi:[1,0]
	v_pk_mul_f32 v[98:99], v[50:51], v[42:43] op_sel_hi:[1,0]
	v_pk_mul_f32 v[100:101], v[4:5], v[76:77] op_sel_hi:[1,0]
	v_pk_mov_b32 v[4:5], v[86:87], v[84:85] op_sel:[1,0]
	v_mov_b32_e32 v87, v85
	v_pk_add_f32 v[4:5], v[4:5], v[86:87]
	v_pk_mul_f32 v[102:103], v[6:7], v[76:77] op_sel_hi:[1,0]
	v_pk_add_f32 v[104:105], v[4:5], v[4:5] op_sel:[0,1] op_sel_hi:[1,0]
	v_cvt_pk_bf16_f32 v7, v40, v41
	ds_read_b128 v[84:87], v150 offset:52224
	ds_read_b128 v[50:53], v150 offset:35840
	ds_read_b128 v[54:57], v150 offset:36864
	ds_read_b128 v[58:61], v150 offset:37888
	ds_read_b128 v[62:65], v150 offset:38912
	v_cvt_pk_bf16_f32 v6, v38, v39
	v_cvt_pk_bf16_f32 v5, v36, v37
	v_cvt_pk_bf16_f32 v4, v34, v35
	ds_read_b128 v[88:91], v150 offset:53248
	ds_read_b128 v[34:37], v150 offset:39936
	ds_read_b128 v[38:41], v150 offset:40960
	ds_read_b128 v[42:45], v150 offset:41984
	ds_read_b128 v[46:49], v150 offset:43008
	v_cvt_pk_bf16_f32 v95, v94, v95
	v_cvt_pk_bf16_f32 v94, v96, v97
	v_cvt_pk_bf16_f32 v93, v92, v93
	v_cvt_pk_bf16_f32 v92, v98, v99
	s_waitcnt lgkmcnt(5)
	v_mfma_f32_32x32x16_bf16 v[50:65], v[84:87], v[4:7], v[50:65]
	v_mul_f32_e32 v10, v10, v76
	v_mul_f32_e32 v11, v11, v76
	v_mul_f32_e32 v12, v12, v76
	v_mul_f32_e32 v13, v13, v76
	v_mul_f32_e32 v8, v8, v76
	v_mul_f32_e32 v9, v9, v76
	v_mov_b32_e32 v77, v104
	s_nop 1
	v_permlane32_swap_b32_e32 v104, v77
	v_cvt_pk_bf16_f32 v73, v72, v73
	s_waitcnt lgkmcnt(0)
	v_mfma_f32_32x32x16_bf16 v[34:49], v[84:87], v[92:95], v[34:49]
	v_cvt_pk_bf16_f32 v72, v70, v71
	v_cvt_pk_bf16_f32 v70, v66, v67
	v_add_f32_e32 v66, v104, v77
	v_cvt_pk_bf16_f32 v71, v68, v69
	v_rcp_f32_e32 v104, v66
	v_cvt_pk_bf16_f32 v69, v82, v83
	v_cvt_pk_bf16_f32 v68, v80, v81
	v_cvt_pk_bf16_f32 v67, v78, v79
	v_cvt_pk_bf16_f32 v66, v74, v75
	ds_read_b128 v[78:81], v150 offset:54272
	v_mfma_f32_32x32x16_bf16 v[50:65], v[88:91], v[70:73], v[50:65]
	v_mul_f32_e32 v2, v2, v76
	v_mul_f32_e32 v3, v3, v76
	v_mul_f32_e32 v20, v20, v104
	v_mul_f32_e32 v21, v21, v104
	v_cvt_pk_bf16_f32 v85, v8, v9
	v_cvt_pk_bf16_f32 v82, v2, v3
	v_pk_mul_f32 v[2:3], v[22:23], v[104:105] op_sel_hi:[1,0]
	v_pk_mul_f32 v[8:9], v[24:25], v[104:105] op_sel_hi:[1,0]
	v_pk_mul_f32 v[18:19], v[18:19], v[104:105] op_sel_hi:[1,0]
	v_mfma_f32_32x32x16_bf16 v[34:49], v[88:91], v[66:69], v[34:49]
	v_cvt_pk_bf16_f32 v84, v102, v103
	v_cvt_pk_bf16_f32 v83, v100, v101
	ds_read_b128 v[86:89], v150 offset:55296
	v_cvt_pk_bf16_f32 v99, v8, v9
	v_cvt_pk_bf16_f32 v98, v2, v3
	v_cvt_pk_bf16_f32 v97, v20, v21
	v_cvt_pk_bf16_f32 v96, v18, v19
	s_waitcnt lgkmcnt(1)
	v_mfma_f32_32x32x16_bf16 v[50:65], v[78:81], v[82:85], v[50:65]
	v_mul_f32_e32 v2, v14, v76
	v_mul_f32_e32 v3, v15, v76
	v_mul_f32_e32 v8, v16, v76
	v_mul_f32_e32 v9, v17, v76
	v_mul_f32_e32 v14, v26, v104
	v_mul_f32_e32 v15, v27, v104
	v_cvt_pk_bf16_f32 v77, v8, v9
	v_cvt_pk_bf16_f32 v76, v2, v3
	v_cvt_pk_bf16_f32 v74, v10, v11
	v_pk_mul_f32 v[2:3], v[28:29], v[104:105] op_sel_hi:[1,0]
	v_mfma_f32_32x32x16_bf16 v[34:49], v[78:81], v[96:99], v[34:49]
	v_mul_f32_e32 v8, v30, v104
	v_mul_f32_e32 v9, v31, v104
	v_mul_f32_e32 v10, v32, v104
	v_mul_f32_e32 v11, v33, v104
	v_cvt_pk_bf16_f32 v75, v12, v13
	v_cvt_pk_bf16_f32 v81, v10, v11
	v_cvt_pk_bf16_f32 v80, v8, v9
	v_cvt_pk_bf16_f32 v79, v2, v3
	v_cvt_pk_bf16_f32 v78, v14, v15
	s_waitcnt lgkmcnt(0)
	v_mfma_f32_32x32x16_bf16 v[50:65], v[86:89], v[74:77], v[50:65]
	v_mfma_f32_32x32x16_bf16 v[34:49], v[86:89], v[78:81], v[34:49]
	ds_read_b128 v[86:89], v150 offset:56320
	ds_read_b128 v[18:21], v150 offset:44032
	ds_read_b128 v[22:25], v150 offset:45056
	ds_read_b128 v[26:29], v150 offset:46080
	ds_read_b128 v[30:33], v150 offset:47104
	ds_read_b128 v[100:103], v150 offset:57344
	s_waitcnt lgkmcnt(1)
	v_mfma_f32_32x32x16_bf16 v[18:33], v[86:89], v[4:7], v[18:33]
	ds_read_b128 v[2:5], v150 offset:48128
	ds_read_b128 v[6:9], v150 offset:49152
	ds_read_b128 v[10:13], v150 offset:50176
	ds_read_b128 v[14:17], v150 offset:51200
	s_waitcnt lgkmcnt(0)
	v_mfma_f32_32x32x16_bf16 v[2:17], v[86:89], v[92:95], v[2:17]
	v_mfma_f32_32x32x16_bf16 v[18:33], v[100:103], v[70:73], v[18:33]
	v_mfma_f32_32x32x16_bf16 v[2:17], v[100:103], v[66:69], v[2:17]
	ds_read_b128 v[66:69], v150 offset:58368
	ds_read_b128 v[70:73], v150 offset:59392
	s_waitcnt lgkmcnt(1)
	v_mfma_f32_32x32x16_bf16 v[18:33], v[66:69], v[82:85], v[18:33]
	v_mfma_f32_32x32x16_bf16 v[2:17], v[66:69], v[96:99], v[2:17]
	s_waitcnt lgkmcnt(0)
	v_mfma_f32_32x32x16_bf16 v[18:33], v[70:73], v[74:77], v[18:33]
	v_mfma_f32_32x32x16_bf16 v[2:17], v[70:73], v[78:81], v[2:17]
	s_nop 10
	v_mul_f32_e32 v66, v22, v22
	v_mul_f32_e32 v67, v23, v23
	v_mul_f32_e32 v68, v30, v30
	v_mul_f32_e32 v69, v31, v31
	v_mul_f32_e32 v70, v24, v24
	v_mul_f32_e32 v71, v25, v25
	v_pk_mul_f32 v[72:73], v[32:33], v[32:33]
	v_pk_mul_f32 v[74:75], v[20:21], v[20:21]
	v_pk_mul_f32 v[76:77], v[28:29], v[28:29]
	v_pk_mul_f32 v[78:79], v[26:27], v[26:27]
	v_pk_mul_f32 v[80:81], v[18:19], v[18:19]
	v_pk_fma_f32 v[78:79], v[58:59], v[58:59], v[78:79]
	v_pk_fma_f32 v[76:77], v[60:61], v[60:61], v[76:77]
	v_pk_fma_f32 v[74:75], v[52:53], v[52:53], v[74:75]
	v_pk_fma_f32 v[72:73], v[64:65], v[64:65], v[72:73]
	v_pk_fma_f32 v[70:71], v[56:57], v[56:57], v[70:71]
	v_pk_fma_f32 v[68:69], v[62:63], v[62:63], v[68:69]
	v_pk_fma_f32 v[66:67], v[54:55], v[54:55], v[66:67]
	v_pk_fma_f32 v[80:81], v[50:51], v[50:51], v[80:81]
	v_pk_add_f32 v[66:67], v[66:67], v[68:69]
	v_pk_add_f32 v[68:69], v[70:71], v[72:73]
	v_pk_add_f32 v[70:71], v[74:75], v[76:77]
	v_pk_add_f32 v[72:73], v[80:81], v[78:79]
	v_pk_add_f32 v[68:69], v[70:71], v[68:69]
	v_pk_add_f32 v[66:67], v[72:73], v[66:67]
	v_pk_mul_f32 v[72:73], v[14:15], v[14:15]
	v_pk_mov_b32 v[70:71], v[66:67], v[68:69] op_sel:[1,0]
	v_mov_b32_e32 v67, v69
	v_pk_add_f32 v[66:67], v[70:71], v[66:67]
	v_pk_mul_f32 v[70:71], v[6:7], v[6:7]
	v_pk_mul_f32 v[74:75], v[8:9], v[8:9]
	v_pk_mul_f32 v[76:77], v[16:17], v[16:17]
	v_pk_mul_f32 v[78:79], v[4:5], v[4:5]
	v_pk_mul_f32 v[80:81], v[12:13], v[12:13]
	v_pk_mul_f32 v[82:83], v[10:11], v[10:11]
	v_pk_mul_f32 v[84:85], v[2:3], v[2:3]
	v_pk_fma_f32 v[82:83], v[42:43], v[42:43], v[82:83]
	v_pk_fma_f32 v[80:81], v[44:45], v[44:45], v[80:81]
	v_pk_fma_f32 v[78:79], v[36:37], v[36:37], v[78:79]
	v_pk_fma_f32 v[76:77], v[48:49], v[48:49], v[76:77]
	v_pk_fma_f32 v[74:75], v[40:41], v[40:41], v[74:75]
	v_pk_fma_f32 v[72:73], v[46:47], v[46:47], v[72:73]
	v_pk_fma_f32 v[70:71], v[38:39], v[38:39], v[70:71]
	v_pk_fma_f32 v[84:85], v[34:35], v[34:35], v[84:85]
	v_pk_add_f32 v[70:71], v[70:71], v[72:73]
	v_pk_add_f32 v[72:73], v[74:75], v[76:77]
	v_pk_add_f32 v[74:75], v[78:79], v[80:81]
	v_pk_add_f32 v[76:77], v[84:85], v[82:83]
	v_pk_add_f32 v[72:73], v[74:75], v[72:73]
	v_pk_add_f32 v[70:71], v[76:77], v[70:71]
	v_pk_add_f32 v[66:67], v[66:67], v[66:67] op_sel:[0,1] op_sel_hi:[1,0]
	v_pk_mov_b32 v[74:75], v[70:71], v[72:73] op_sel:[1,0]
	v_mov_b32_e32 v71, v73
	v_pk_add_f32 v[70:71], v[74:75], v[70:71]
	v_mov_b32_e32 v69, v66
	v_pk_add_f32 v[70:71], v[70:71], v[70:71] op_sel:[0,1] op_sel_hi:[1,0]
	s_nop 0
	v_permlane32_swap_b32_e32 v66, v69
	v_mov_b32_e32 v68, v70
	s_nop 1
	v_permlane32_swap_b32_e32 v70, v68
	v_mov_b32_e32 v71, v66
	v_pk_add_f32 v[66:67], v[70:71], v[68:69]
	v_pk_fma_f32 v[66:67], v[66:67], s[0:1], v[152:153] op_sel_hi:[1,0,0]
	s_mov_b32 s1, 0x800000
	v_mul_f32_e32 v68, 0x4b800000, v67
	v_cmp_gt_f32_e32 vcc, s1, v67
	s_nop 1
	v_cndmask_b32_e32 v67, v67, v68, vcc
	v_rsq_f32_e32 v67, v67
	s_nop 0
	v_mul_f32_e32 v68, 0x45800000, v67
	v_cndmask_b32_e32 v68, v67, v68, vcc
	v_pk_mul_f32 v[158:159], v[50:51], v[68:69] op_sel_hi:[1,0]
	v_pk_mul_f32 v[50:51], v[18:19], v[68:69] op_sel_hi:[1,0]
	v_mul_f32_e32 v18, 0x4b800000, v66
	v_cmp_gt_f32_e32 vcc, s1, v66
	v_pk_mul_f32 v[80:81], v[60:61], v[68:69] op_sel_hi:[1,0]
	v_pk_mul_f32 v[60:61], v[28:29], v[68:69] op_sel_hi:[1,0]
	v_cndmask_b32_e32 v18, v66, v18, vcc
	v_rsq_f32_e32 v18, v18
	v_pk_mul_f32 v[78:79], v[58:59], v[68:69] op_sel_hi:[1,0]
	v_pk_mul_f32 v[160:161], v[52:53], v[68:69] op_sel_hi:[1,0]
	v_pk_mul_f32 v[82:83], v[54:55], v[68:69] op_sel_hi:[1,0]
	v_mul_f32_e32 v19, 0x45800000, v18
	v_cndmask_b32_e32 v28, v18, v19, vcc
	v_pk_mul_f32 v[168:169], v[56:57], v[68:69] op_sel_hi:[1,0]
	v_pk_mul_f32 v[58:59], v[26:27], v[68:69] op_sel_hi:[1,0]
	v_pk_mul_f32 v[52:53], v[20:21], v[68:69] op_sel_hi:[1,0]
	v_pk_mul_f32 v[54:55], v[22:23], v[68:69] op_sel_hi:[1,0]
	v_pk_mul_f32 v[56:57], v[24:25], v[68:69] op_sel_hi:[1,0]
	v_pk_mul_f32 v[18:19], v[42:43], v[28:29] op_sel_hi:[1,0]
	v_pk_mul_f32 v[20:21], v[44:45], v[28:29] op_sel_hi:[1,0]
	v_pk_mul_f32 v[22:23], v[46:47], v[28:29] op_sel_hi:[1,0]
	v_pk_mul_f32 v[26:27], v[48:49], v[28:29] op_sel_hi:[1,0]
	v_pk_mul_f32 v[162:163], v[34:35], v[28:29] op_sel_hi:[1,0]
	v_pk_mul_f32 v[164:165], v[36:37], v[28:29] op_sel_hi:[1,0]
	v_pk_mul_f32 v[166:167], v[38:39], v[28:29] op_sel_hi:[1,0]
	v_pk_mul_f32 v[24:25], v[40:41], v[28:29] op_sel_hi:[1,0]
	v_pk_mul_f32 v[104:105], v[2:3], v[28:29] op_sel_hi:[1,0]
	v_pk_mul_f32 v[112:113], v[4:5], v[28:29] op_sel_hi:[1,0]
	s_nop 0
	s_nop 0
	ds_read_b128 v[2:5], v150 offset:60416
	ds_read_b128 v[34:37], v174 offset:32768
	ds_read_b128 v[38:41], v174 offset:32800
	ds_read_b128 v[42:45], v174 offset:32832
	ds_read_b128 v[46:49], v174 offset:32864
	v_cvt_pk_bf16_f32 v129, v168, v169
	v_cvt_pk_bf16_f32 v128, v82, v83
	v_cvt_pk_bf16_f32 v127, v160, v161
	v_cvt_pk_bf16_f32 v126, v158, v159
	v_cvt_pk_bf16_f32 v137, v24, v25
	v_cvt_pk_bf16_f32 v136, v166, v167
	v_cvt_pk_bf16_f32 v135, v164, v165
	s_waitcnt lgkmcnt(0)
	v_mfma_f32_32x32x16_bf16 v[86:101], v[2:5], v[126:129], v[34:49]
	v_cvt_pk_bf16_f32 v134, v162, v163
	v_mul_f32_e32 v84, v62, v68
	v_mul_f32_e32 v85, v63, v68
	v_mul_f32_e32 v170, v64, v68
	v_mul_f32_e32 v171, v65, v68
	v_pk_mul_f32 v[62:63], v[30:31], v[68:69] op_sel_hi:[1,0]
	v_pk_mul_f32 v[64:65], v[32:33], v[68:69] op_sel_hi:[1,0]
	v_pk_mul_f32 v[116:117], v[6:7], v[28:29] op_sel_hi:[1,0]
	v_pk_mul_f32 v[154:155], v[8:9], v[28:29] op_sel_hi:[1,0]
	v_mfma_f32_32x32x16_bf16 v[34:49], v[2:5], v[134:137], v[34:49]
	ds_read_b128 v[6:9], v150 offset:61440
	ds_read_b128 v[66:69], v174 offset:32896
	ds_read_b128 v[106:109], v150 offset:64512
	v_cvt_pk_bf16_f32 v125, v170, v171
	v_cvt_pk_bf16_f32 v124, v84, v85
	v_cvt_pk_bf16_f32 v123, v80, v81
	v_cvt_pk_bf16_f32 v122, v78, v79
	v_cvt_pk_bf16_f32 v149, v26, v27
	v_cvt_pk_bf16_f32 v148, v22, v23
	v_cvt_pk_bf16_f32 v147, v20, v21
	v_cvt_pk_bf16_f32 v146, v18, v19
	s_waitcnt lgkmcnt(2)
	v_mfma_f32_32x32x16_bf16 v[86:101], v[6:9], v[122:125], v[86:101]
	v_mul_f32_e32 v102, v10, v28
	v_mul_f32_e32 v103, v11, v28
	v_mul_f32_e32 v110, v12, v28
	v_mul_f32_e32 v111, v13, v28
	v_mul_f32_e32 v114, v14, v28
	v_mul_f32_e32 v115, v15, v28
	v_pk_mul_f32 v[156:157], v[16:17], v[28:29] op_sel_hi:[1,0]
	ds_read_b128 v[176:179], v174 offset:33536
	ds_read_b128 v[180:183], v174 offset:33568
	ds_read_b128 v[184:187], v174 offset:33600
	ds_read_b128 v[28:31], v174 offset:33632
	ds_read_b128 v[188:191], v174 offset:33792
	ds_read_b128 v[192:195], v174 offset:33824
	ds_read_b128 v[196:199], v174 offset:33856
	ds_read_b128 v[200:203], v174 offset:33888
	ds_read_b128 v[204:207], v150 offset:62464
	v_cvt_pk_bf16_f32 v133, v56, v57
	v_mfma_f32_32x32x16_bf16 v[34:49], v[6:9], v[146:149], v[34:49]
	v_cvt_pk_bf16_f32 v132, v54, v55
	v_cvt_pk_bf16_f32 v131, v52, v53
	v_cvt_pk_bf16_f32 v130, v50, v51
	ds_read_b128 v[70:73], v174 offset:33664
	ds_read_b128 v[74:77], v174 offset:33920
	ds_read_b128 v[208:211], v150 offset:63488
	v_cvt_pk_bf16_f32 v145, v154, v155
	v_cvt_pk_bf16_f32 v144, v116, v117
	v_cvt_pk_bf16_f32 v143, v112, v113
	v_cvt_pk_bf16_f32 v142, v104, v105
	s_waitcnt lgkmcnt(3)
	v_mfma_f32_32x32x16_bf16 v[86:101], v[204:207], v[130:133], v[86:101]
	v_cvt_pk_bf16_f32 v121, v64, v65
	v_cvt_pk_bf16_f32 v120, v62, v63
	v_cvt_pk_bf16_f32 v119, v60, v61
	v_cvt_pk_bf16_f32 v118, v58, v59
	v_cvt_pk_bf16_f32 v141, v156, v157
	v_cvt_pk_bf16_f32 v140, v114, v115
	v_cvt_pk_bf16_f32 v139, v110, v111
	v_mfma_f32_32x32x16_bf16 v[34:49], v[204:207], v[142:145], v[34:49]
	v_cvt_pk_bf16_f32 v138, v102, v103
	v_fma_f32 v16, v30, v170, v202
	v_fma_f32 v17, v31, v171, v203
	v_fma_f32 v14, v28, v84, v200
	v_fma_f32 v15, v29, v85, v201
	v_pk_fma_f32 v[12:13], v[186:187], v[80:81], v[198:199]
	v_pk_fma_f32 v[10:11], v[184:185], v[78:79], v[196:197]
	v_pk_fma_f32 v[8:9], v[182:183], v[168:169], v[194:195]
	s_waitcnt lgkmcnt(0)
	v_mfma_f32_32x32x16_bf16 v[86:101], v[208:211], v[118:121], v[86:101]
	v_fma_f32 v6, v180, v82, v192
	v_fma_f32 v7, v181, v83, v193
	ds_read_b128 v[78:81], v174 offset:33760
	ds_read_b128 v[82:85], v174 offset:33248
	v_fma_f32 v4, v178, v160, v190
	v_fma_f32 v5, v179, v161, v191
	v_pk_fma_f32 v[2:3], v[176:177], v[158:159], v[188:189]
	v_pk_fma_f32 v[32:33], v[30:31], v[26:27], v[202:203]
	v_pk_fma_f32 v[30:31], v[28:29], v[22:23], v[200:201]
	v_pk_fma_f32 v[28:29], v[186:187], v[20:21], v[198:199]
	v_pk_fma_f32 v[26:27], v[184:185], v[18:19], v[196:197]
	v_pk_fma_f32 v[24:25], v[182:183], v[24:25], v[194:195]
	v_pk_fma_f32 v[22:23], v[180:181], v[166:167], v[192:193]
	v_pk_fma_f32 v[20:21], v[178:179], v[164:165], v[190:191]
	v_pk_fma_f32 v[18:19], v[176:177], v[162:163], v[188:189]
	ds_read_b128 v[158:161], v174 offset:33696
	ds_read_b128 v[162:165], v174 offset:33728
	ds_read_b128 v[166:169], v174 offset:33952
	ds_read_b128 v[176:179], v174 offset:33984
	ds_read_b128 v[180:183], v174 offset:34016
	ds_read_b128 v[184:187], v212 offset:11264
	v_mfma_f32_32x32x16_bf16 v[34:49], v[208:211], v[138:141], v[34:49]
	v_cvt_pk_bf16_f32 v86, v86, v87
	v_cvt_pk_bf16_f32 v87, v88, v89
	v_cvt_pk_bf16_f32 v88, v90, v91
	v_cvt_pk_bf16_f32 v89, v92, v93
	ds_read_b128 v[90:93], v212 offset:12288
	v_pk_max_i16 v86, v86, 0
	v_pk_max_i16 v87, v87, 0
	v_pk_max_i16 v88, v88, 0
	v_pk_max_i16 v89, v89, 0
	s_nop 1
	s_nop 0
	v_cvt_pk_bf16_f32 v188, v34, v35
	v_cvt_pk_bf16_f32 v189, v36, v37
	v_cvt_pk_bf16_f32 v190, v38, v39
	v_cvt_pk_bf16_f32 v191, v40, v41
	s_waitcnt lgkmcnt(1)
	v_mfma_f32_32x32x16_bf16 v[2:17], v[184:187], v[86:89], v[2:17]
	v_pk_max_i16 v188, v188, 0
	v_pk_max_i16 v189, v189, 0
	v_pk_max_i16 v190, v190, 0
	v_pk_max_i16 v191, v191, 0
	v_cvt_pk_bf16_f32 v94, v94, v95
	v_cvt_pk_bf16_f32 v95, v96, v97
	v_cvt_pk_bf16_f32 v96, v98, v99
	v_cvt_pk_bf16_f32 v97, v100, v101
	v_cvt_pk_bf16_f32 v98, v42, v43
	v_cvt_pk_bf16_f32 v99, v44, v45
	v_mfma_f32_32x32x16_bf16 v[18:33], v[184:187], v[188:191], v[18:33]
	ds_read_b128 v[184:187], v212 offset:19456
	v_cvt_pk_bf16_f32 v100, v46, v47
	v_cvt_pk_bf16_f32 v101, v48, v49
	v_fma_f32 v64, v80, v64, v182
	v_fma_f32 v65, v81, v65, v183
	v_pk_fma_f32 v[62:63], v[78:79], v[62:63], v[180:181]
	v_pk_fma_f32 v[60:61], v[164:165], v[60:61], v[178:179]
	v_pk_fma_f32 v[58:59], v[162:163], v[58:59], v[176:177]
	v_pk_max_i16 v94, v94, 0
	v_pk_max_i16 v95, v95, 0
	v_pk_max_i16 v96, v96, 0
	v_pk_max_i16 v97, v97, 0
	v_pk_max_i16 v98, v98, 0
	v_pk_max_i16 v99, v99, 0
	v_pk_max_i16 v100, v100, 0
	v_pk_max_i16 v101, v101, 0
	v_pk_fma_f32 v[56:57], v[160:161], v[56:57], v[168:169]
	s_waitcnt lgkmcnt(1)
	v_mfma_f32_32x32x16_bf16 v[2:17], v[90:93], v[94:97], v[2:17]
	v_fma_f32 v54, v158, v54, v166
	v_fma_f32 v55, v159, v55, v167
	v_fma_f32 v52, v72, v52, v76
	v_fma_f32 v53, v73, v53, v77
	v_fma_f32 v50, v70, v50, v74
	v_fma_f32 v51, v71, v51, v75
	v_pk_fma_f32 v[48:49], v[80:81], v[156:157], v[182:183]
	v_pk_fma_f32 v[46:47], v[78:79], v[114:115], v[180:181]
	v_pk_fma_f32 v[44:45], v[164:165], v[110:111], v[178:179]
	v_pk_fma_f32 v[42:43], v[162:163], v[102:103], v[176:177]
	v_mfma_f32_32x32x16_bf16 v[18:33], v[90:93], v[98:101], v[18:33]
	ds_read_b128 v[90:93], v212 offset:20480
	v_fma_f32 v40, v160, v154, v168
	v_fma_f32 v41, v161, v155, v169
	v_fma_f32 v38, v158, v116, v166
	v_fma_f32 v39, v159, v117, v167
	v_pk_fma_f32 v[36:37], v[72:73], v[112:113], v[76:77]
	v_pk_fma_f32 v[34:35], v[70:71], v[104:105], v[74:75]
	s_waitcnt lgkmcnt(1)
	v_mfma_f32_32x32x16_bf16 v[50:65], v[184:187], v[86:89], v[50:65]
	ds_read_b128 v[70:73], v174 offset:32928
	ds_read_b128 v[74:77], v174 offset:32960
	ds_read_b128 v[78:81], v174 offset:32992
	ds_read_b128 v[86:89], v174 offset:33024
	ds_read_b128 v[110:113], v212 offset:1024
	v_mfma_f32_32x32x16_bf16 v[34:49], v[184:187], v[188:191], v[34:49]
	s_waitcnt lgkmcnt(5)
	v_mfma_f32_32x32x16_bf16 v[50:65], v[90:93], v[94:97], v[50:65]
	v_mfma_f32_32x32x16_bf16 v[34:49], v[90:93], v[98:101], v[34:49]
	s_waitcnt lgkmcnt(2)
	v_mfma_f32_32x32x16_bf16 v[90:105], v[106:109], v[126:129], v[66:81]
	v_mfma_f32_32x32x16_bf16 v[66:81], v[106:109], v[134:137], v[66:81]
	ds_read_b128 v[106:109], v212 offset:0
	s_waitcnt lgkmcnt(0)
	v_mfma_f32_32x32x16_bf16 v[90:105], v[106:109], v[122:125], v[90:105]
	v_mfma_f32_32x32x16_bf16 v[66:81], v[106:109], v[146:149], v[66:81]
	ds_read_b128 v[106:109], v212 offset:2048
	v_mfma_f32_32x32x16_bf16 v[90:105], v[110:113], v[130:133], v[90:105]
	v_mfma_f32_32x32x16_bf16 v[66:81], v[110:113], v[142:145], v[66:81]
	ds_read_b128 v[110:113], v212 offset:13312
	s_waitcnt lgkmcnt(1)
	v_mfma_f32_32x32x16_bf16 v[90:105], v[106:109], v[118:121], v[90:105]
	v_mfma_f32_32x32x16_bf16 v[66:81], v[106:109], v[138:141], v[66:81]
	s_nop 10
	v_cvt_pk_bf16_f32 v90, v90, v91
	v_cvt_pk_bf16_f32 v91, v92, v93
	v_cvt_pk_bf16_f32 v92, v94, v95
	v_cvt_pk_bf16_f32 v94, v98, v99
	v_cvt_pk_bf16_f32 v95, v100, v101
	ds_read_b128 v[98:101], v212 offset:21504
	v_cvt_pk_bf16_f32 v66, v66, v67
	v_cvt_pk_bf16_f32 v67, v68, v69
	v_cvt_pk_bf16_f32 v68, v70, v71
	v_cvt_pk_bf16_f32 v93, v96, v97
	v_cvt_pk_bf16_f32 v69, v72, v73
	ds_read_b128 v[70:73], v212 offset:14336
	v_pk_max_i16 v90, v90, 0
	v_pk_max_i16 v91, v91, 0
	v_pk_max_i16 v92, v92, 0
	v_pk_max_i16 v93, v93, 0
	v_pk_max_i16 v66, v66, 0
	v_pk_max_i16 v67, v67, 0
	v_pk_max_i16 v68, v68, 0
	v_pk_max_i16 v69, v69, 0
	v_cvt_pk_bf16_f32 v96, v102, v103
	s_waitcnt lgkmcnt(2)
	v_mfma_f32_32x32x16_bf16 v[2:17], v[110:113], v[90:93], v[2:17]
	v_cvt_pk_bf16_f32 v97, v104, v105
	v_cvt_pk_bf16_f32 v74, v74, v75
	v_cvt_pk_bf16_f32 v75, v76, v77
	v_cvt_pk_bf16_f32 v76, v78, v79
	v_cvt_pk_bf16_f32 v77, v80, v81
	v_pk_max_i16 v94, v94, 0
	v_pk_max_i16 v95, v95, 0
	v_pk_max_i16 v96, v96, 0
	v_pk_max_i16 v97, v97, 0
	v_pk_max_i16 v74, v74, 0
	v_pk_max_i16 v75, v75, 0
	v_pk_max_i16 v76, v76, 0
	v_pk_max_i16 v77, v77, 0
	v_mfma_f32_32x32x16_bf16 v[18:33], v[110:113], v[66:69], v[18:33]
	s_waitcnt lgkmcnt(1)
	v_mfma_f32_32x32x16_bf16 v[34:49], v[98:101], v[66:69], v[34:49]
	ds_read_b128 v[66:69], v212 offset:22528
	v_mfma_f32_32x32x16_bf16 v[50:65], v[98:101], v[90:93], v[50:65]
	s_waitcnt lgkmcnt(1)
	v_mfma_f32_32x32x16_bf16 v[2:17], v[70:73], v[94:97], v[2:17]
	v_mfma_f32_32x32x16_bf16 v[18:33], v[70:73], v[74:77], v[18:33]
	ds_read_b128 v[78:81], v212 offset:3072
	s_waitcnt lgkmcnt(1)
	v_mfma_f32_32x32x16_bf16 v[50:65], v[66:69], v[94:97], v[50:65]
	ds_read_b128 v[90:93], v174 offset:33056
	ds_read_b128 v[94:97], v174 offset:33088
	ds_read_b128 v[98:101], v174 offset:33120
	ds_read_b128 v[70:73], v174 offset:33152
	v_mfma_f32_32x32x16_bf16 v[34:49], v[66:69], v[74:77], v[34:49]
	ds_read_b128 v[66:69], v212 offset:4096
	ds_read_b128 v[74:77], v212 offset:5120
	s_waitcnt lgkmcnt(3)
	v_mfma_f32_32x32x16_bf16 v[102:117], v[78:81], v[126:129], v[86:101]
	v_mfma_f32_32x32x16_bf16 v[86:101], v[78:81], v[134:137], v[86:101]
	s_waitcnt lgkmcnt(1)
	v_mfma_f32_32x32x16_bf16 v[86:101], v[66:69], v[146:149], v[86:101]
	v_mfma_f32_32x32x16_bf16 v[102:117], v[66:69], v[122:125], v[102:117]
	ds_read_b128 v[66:69], v212 offset:6144
	s_waitcnt lgkmcnt(1)
	v_mfma_f32_32x32x16_bf16 v[86:101], v[74:77], v[142:145], v[86:101]
	v_mfma_f32_32x32x16_bf16 v[102:117], v[74:77], v[130:133], v[102:117]
	ds_read_b128 v[74:77], v212 offset:15360
	s_waitcnt lgkmcnt(1)
	v_mfma_f32_32x32x16_bf16 v[86:101], v[66:69], v[138:141], v[86:101]
	v_mfma_f32_32x32x16_bf16 v[102:117], v[66:69], v[118:121], v[102:117]
	s_nop 10
	v_cvt_pk_bf16_f32 v78, v86, v87
	v_cvt_pk_bf16_f32 v80, v90, v91
	v_cvt_pk_bf16_f32 v79, v88, v89
	v_cvt_pk_bf16_f32 v81, v92, v93
	ds_read_b128 v[86:89], v212 offset:16384
	ds_read_b128 v[90:93], v212 offset:23552
	v_cvt_pk_bf16_f32 v66, v102, v103
	v_cvt_pk_bf16_f32 v67, v104, v105
	v_cvt_pk_bf16_f32 v68, v106, v107
	v_cvt_pk_bf16_f32 v69, v108, v109
	v_pk_max_i16 v66, v66, 0
	v_pk_max_i16 v67, v67, 0
	v_pk_max_i16 v68, v68, 0
	v_pk_max_i16 v69, v69, 0
	v_pk_max_i16 v78, v78, 0
	v_pk_max_i16 v79, v79, 0
	v_pk_max_i16 v80, v80, 0
	v_pk_max_i16 v81, v81, 0
	v_cvt_pk_bf16_f32 v94, v94, v95
	s_waitcnt lgkmcnt(2)
	v_mfma_f32_32x32x16_bf16 v[18:33], v[74:77], v[78:81], v[18:33]
	v_cvt_pk_bf16_f32 v95, v96, v97
	v_cvt_pk_bf16_f32 v96, v98, v99
	v_cvt_pk_bf16_f32 v97, v100, v101
	v_pk_max_i16 v94, v94, 0
	v_pk_max_i16 v95, v95, 0
	v_pk_max_i16 v96, v96, 0
	v_pk_max_i16 v97, v97, 0
	v_mfma_f32_32x32x16_bf16 v[2:17], v[74:77], v[66:69], v[2:17]
	v_cvt_pk_bf16_f32 v74, v110, v111
	v_cvt_pk_bf16_f32 v75, v112, v113
	v_cvt_pk_bf16_f32 v76, v114, v115
	v_cvt_pk_bf16_f32 v77, v116, v117
	v_pk_max_i16 v74, v74, 0
	v_pk_max_i16 v75, v75, 0
	v_pk_max_i16 v76, v76, 0
	v_pk_max_i16 v77, v77, 0
	s_waitcnt lgkmcnt(0)
	v_mfma_f32_32x32x16_bf16 v[50:65], v[90:93], v[66:69], v[50:65]
	ds_read_b128 v[66:69], v212 offset:24576
	v_mfma_f32_32x32x16_bf16 v[34:49], v[90:93], v[78:81], v[34:49]
	ds_read_b128 v[102:105], v212 offset:7168
	v_mfma_f32_32x32x16_bf16 v[2:17], v[86:89], v[74:77], v[2:17]
	s_waitcnt lgkmcnt(1)
	v_mfma_f32_32x32x16_bf16 v[50:65], v[66:69], v[74:77], v[50:65]
	ds_read_b128 v[74:77], v174 offset:33184
	ds_read_b128 v[78:81], v174 offset:33216
	v_mfma_f32_32x32x16_bf16 v[34:49], v[66:69], v[94:97], v[34:49]
	ds_read_b128 v[66:69], v212 offset:8192
	v_mfma_f32_32x32x16_bf16 v[18:33], v[86:89], v[94:97], v[18:33]
	s_waitcnt lgkmcnt(1)
	v_mfma_f32_32x32x16_bf16 v[86:101], v[102:105], v[126:129], v[70:85]
	v_mfma_f32_32x32x16_bf16 v[70:85], v[102:105], v[134:137], v[70:85]
	ds_read_b128 v[102:105], v212 offset:9216
	v_lshlrev_b32_e32 v135, 2, v1
	v_add_u32_e32 v134, v172, v174
	s_waitcnt lgkmcnt(1)
	v_mfma_f32_32x32x16_bf16 v[86:101], v[66:69], v[122:125], v[86:101]
	v_mfma_f32_32x32x16_bf16 v[70:85], v[66:69], v[146:149], v[70:85]
	ds_read_b128 v[66:69], v212 offset:10240
	s_waitcnt lgkmcnt(1)
	v_mfma_f32_32x32x16_bf16 v[86:101], v[102:105], v[130:133], v[86:101]
	v_mfma_f32_32x32x16_bf16 v[70:85], v[102:105], v[142:145], v[70:85]
	ds_read_b128 v[102:105], v212 offset:17408
	s_waitcnt lgkmcnt(1)
	v_mfma_f32_32x32x16_bf16 v[86:101], v[66:69], v[118:121], v[86:101]
	v_mfma_f32_32x32x16_bf16 v[70:85], v[66:69], v[138:141], v[70:85]
	s_nop 10
	v_cvt_pk_bf16_f32 v68, v90, v91
	v_cvt_pk_bf16_f32 v69, v92, v93
	ds_read_b128 v[90:93], v212 offset:25600
	v_cvt_pk_bf16_f32 v66, v86, v87
	v_cvt_pk_bf16_f32 v67, v88, v89
	v_pk_max_i16 v66, v66, 0
	v_pk_max_i16 v67, v67, 0
	v_pk_max_i16 v68, v68, 0
	v_pk_max_i16 v69, v69, 0
	v_cvt_pk_bf16_f32 v70, v70, v71
	v_cvt_pk_bf16_f32 v71, v72, v73
	s_waitcnt lgkmcnt(1)
	v_mfma_f32_32x32x16_bf16 v[2:17], v[102:105], v[66:69], v[2:17]
	v_cvt_pk_bf16_f32 v72, v74, v75
	v_cvt_pk_bf16_f32 v73, v76, v77
	ds_read_b128 v[74:77], v212 offset:18432
	v_cvt_pk_bf16_f32 v86, v94, v95
	v_cvt_pk_bf16_f32 v87, v96, v97
	v_cvt_pk_bf16_f32 v88, v98, v99
	s_waitcnt lgkmcnt(1)
	v_mfma_f32_32x32x16_bf16 v[50:65], v[90:93], v[66:69], v[50:65]
	ds_read_b128 v[66:69], v212 offset:26624
	v_cvt_pk_bf16_f32 v89, v100, v101
	v_pk_max_i16 v86, v86, 0
	v_pk_max_i16 v87, v87, 0
	v_pk_max_i16 v88, v88, 0
	v_pk_max_i16 v89, v89, 0
	v_pk_max_i16 v70, v70, 0
	v_pk_max_i16 v71, v71, 0
	v_pk_max_i16 v72, v72, 0
	v_pk_max_i16 v73, v73, 0
	v_cvt_pk_bf16_f32 v78, v78, v79
	v_cvt_pk_bf16_f32 v79, v80, v81
	s_waitcnt lgkmcnt(1)
	v_mfma_f32_32x32x16_bf16 v[2:17], v[74:77], v[86:89], v[2:17]
	v_cvt_pk_bf16_f32 v80, v82, v83
	v_cvt_pk_bf16_f32 v81, v84, v85
	v_pk_max_i16 v78, v78, 0
	v_pk_max_i16 v79, v79, 0
	v_pk_max_i16 v80, v80, 0
	v_pk_max_i16 v81, v81, 0
	s_waitcnt lgkmcnt(0)
	v_mfma_f32_32x32x16_bf16 v[50:65], v[66:69], v[86:89], v[50:65]
	v_mfma_f32_32x32x16_bf16 v[34:49], v[90:93], v[70:73], v[34:49]
	s_nop 10
	v_add_f32_e32 v130, v10, v58
	v_add_f32_e32 v131, v11, v59
	v_add_f32_e32 v132, v12, v60
	v_add_f32_e32 v133, v13, v61
	v_add_f32_e32 v138, v4, v52
	v_add_f32_e32 v139, v5, v53
	v_pk_add_f32 v[140:141], v[16:17], v[64:65]
	v_pk_add_f32 v[142:143], v[8:9], v[56:57]
	v_pk_add_f32 v[144:145], v[14:15], v[62:63]
	v_pk_add_f32 v[146:147], v[6:7], v[54:55]
	v_mfma_f32_32x32x16_bf16 v[18:33], v[102:105], v[70:73], v[18:33]
	ds_read2st64_b32 v[70:71], v135 offset0:133 offset1:134
	v_add_f32_e32 v148, v2, v50
	v_add_f32_e32 v149, v3, v51
	v_add_f32_e32 v144, v146, v144
	v_add_f32_e32 v145, v147, v145
	v_pk_add_f32 v[140:141], v[142:143], v[140:141]
	v_pk_add_f32 v[132:133], v[138:139], v[132:133]
	v_pk_add_f32 v[130:131], v[148:149], v[130:131]
	v_pk_add_f32 v[132:133], v[132:133], v[140:141]
	v_pk_add_f32 v[130:131], v[130:131], v[144:145]
	v_mfma_f32_32x32x16_bf16 v[34:49], v[66:69], v[78:81], v[34:49]
	v_pk_mov_b32 v[138:139], v[130:131], v[132:133] op_sel:[1,0]
	v_mov_b32_e32 v131, v133
	s_waitcnt vmcnt(0) lgkmcnt(0)
	v_mul_f32_e32 v66, v175, v70
	v_pk_add_f32 v[130:131], v[138:139], v[130:131]
	ds_write_b32 v173, v66 offset:512
	v_mul_f32_e32 v66, v175, v71
	v_pk_add_f32 v[130:131], v[130:131], v[130:131] op_sel:[0,1] op_sel_hi:[1,0]
	s_waitcnt lgkmcnt(0)
	ds_read_b128 v[102:105], v174 offset:34560
	ds_read_b128 v[98:101], v174 offset:34592
	ds_read_b128 v[110:113], v174 offset:34624
	ds_read_b128 v[106:109], v174 offset:34656
	ds_read_b128 v[114:117], v174 offset:34688
	ds_read_b128 v[122:125], v174 offset:34720
	ds_read_b128 v[118:121], v174 offset:34752
	ds_read_b128 v[126:129], v174 offset:34784
	v_mov_b32_dpp v66, v66 quad_perm:[1,0,3,2] row_mask:0xf bank_mask:0xf bound_ctrl:1
	v_mov_b32_e32 v131, v130
	v_fmac_f32_e32 v66, v175, v71
	s_nop 0
	v_permlane32_swap_b32_e32 v130, v131
	v_add_f32_dpp v66, v66, v66 quad_perm:[2,3,0,1] row_mask:0xf bank_mask:0xf bound_ctrl:1
	v_add_f32_e32 v130, v130, v131
	v_fmamk_f32 v65, v130, 0xbc800000, v65
	v_add_f32_dpp v66, v66, v66 row_half_mirror row_mask:0xf bank_mask:0xf bound_ctrl:1
	v_fmamk_f32 v64, v130, 0xbc800000, v64
	v_fmamk_f32 v63, v130, 0xbc800000, v63
	v_fmamk_f32 v62, v130, 0xbc800000, v62
	v_fmamk_f32 v61, v130, 0xbc800000, v61
	v_fmamk_f32 v60, v130, 0xbc800000, v60
	v_fmamk_f32 v59, v130, 0xbc800000, v59
	v_fmamk_f32 v58, v130, 0xbc800000, v58
	v_fmamk_f32 v57, v130, 0xbc800000, v57
	v_fmamk_f32 v56, v130, 0xbc800000, v56
	v_fmamk_f32 v55, v130, 0xbc800000, v55
	v_fmamk_f32 v54, v130, 0xbc800000, v54
	v_fmamk_f32 v53, v130, 0xbc800000, v53
	v_fmamk_f32 v52, v130, 0xbc800000, v52
	v_fmamk_f32 v51, v130, 0xbc800000, v51
	v_fmac_f32_e32 v50, 0xbc800000, v130
	v_add_f32_dpp v66, v66, v66 row_ror:8 row_mask:0xf bank_mask:0xf bound_ctrl:1
	v_fmamk_f32 v17, v130, 0xbc800000, v17
	v_fmamk_f32 v16, v130, 0xbc800000, v16
	v_fmamk_f32 v15, v130, 0xbc800000, v15
	v_fmamk_f32 v14, v130, 0xbc800000, v14
	v_fmamk_f32 v13, v130, 0xbc800000, v13
	v_fmamk_f32 v12, v130, 0xbc800000, v12
	v_fmamk_f32 v11, v130, 0xbc800000, v11
	v_fmamk_f32 v10, v130, 0xbc800000, v10
	v_fmamk_f32 v9, v130, 0xbc800000, v9
	v_fmamk_f32 v8, v130, 0xbc800000, v8
	v_fmamk_f32 v7, v130, 0xbc800000, v7
	v_fmamk_f32 v6, v130, 0xbc800000, v6
	v_fmamk_f32 v5, v130, 0xbc800000, v5
	v_fmamk_f32 v4, v130, 0xbc800000, v4
	v_fmamk_f32 v3, v130, 0xbc800000, v3
	v_fmac_f32_e32 v2, 0xbc800000, v130
	v_pk_mul_f32 v[130:131], v[54:55], v[54:55]
	v_pk_mul_f32 v[132:133], v[62:63], v[62:63]
	v_pk_mul_f32 v[138:139], v[50:51], v[50:51]
	v_pk_mul_f32 v[140:141], v[58:59], v[58:59]
	v_pk_mul_f32 v[142:143], v[56:57], v[56:57]
	v_pk_mul_f32 v[144:145], v[64:65], v[64:65]
	v_pk_mul_f32 v[146:147], v[52:53], v[52:53]
	v_pk_mul_f32 v[148:149], v[60:61], v[60:61]
	v_mov_b32_e32 v67, v66
	v_pk_fma_f32 v[148:149], v[12:13], v[12:13], v[148:149]
	v_pk_fma_f32 v[146:147], v[4:5], v[4:5], v[146:147]
	v_pk_fma_f32 v[144:145], v[16:17], v[16:17], v[144:145]
	v_pk_fma_f32 v[142:143], v[8:9], v[8:9], v[142:143]
	v_pk_fma_f32 v[140:141], v[10:11], v[10:11], v[140:141]
	v_pk_fma_f32 v[138:139], v[2:3], v[2:3], v[138:139]
	v_pk_fma_f32 v[132:133], v[14:15], v[14:15], v[132:133]
	v_pk_fma_f32 v[130:131], v[6:7], v[6:7], v[130:131]
	v_permlane16_swap_b32_e32 v66, v67
	v_pk_add_f32 v[130:131], v[130:131], v[132:133]
	v_pk_add_f32 v[132:133], v[138:139], v[140:141]
	v_pk_add_f32 v[138:139], v[142:143], v[144:145]
	v_pk_add_f32 v[140:141], v[146:147], v[148:149]
	v_mfma_f32_32x32x16_bf16 v[18:33], v[74:77], v[78:81], v[18:33]
	v_add_f32_e32 v136, v66, v67
	ds_read_b128 v[70:73], v134 offset:512
	ds_read_b128 v[66:69], v134 offset:544
	ds_read_b128 v[78:81], v134 offset:576
	ds_read_b128 v[74:77], v134 offset:608
	ds_read_b128 v[82:85], v134 offset:640
	ds_read_b128 v[90:93], v134 offset:672
	ds_read_b128 v[86:89], v134 offset:704
	ds_read_b128 v[94:97], v134 offset:736
	v_pk_add_f32 v[138:139], v[140:141], v[138:139]
	v_pk_add_f32 v[130:131], v[132:133], v[130:131]
	s_waitcnt lgkmcnt(8)
	v_pk_mul_f32 v[140:141], v[126:127], v[62:63]
	v_pk_mov_b32 v[132:133], v[130:131], v[138:139] op_sel:[1,0]
	v_mov_b32_e32 v131, v139
	v_pk_mul_f32 v[138:139], v[122:123], v[54:55]
	v_pk_mul_f32 v[142:143], v[114:115], v[50:51]
	v_pk_mul_f32 v[144:145], v[118:119], v[58:59]
	v_pk_mul_f32 v[146:147], v[124:125], v[56:57]
	v_pk_mul_f32 v[148:149], v[128:129], v[64:65]
	v_pk_mul_f32 v[154:155], v[116:117], v[52:53]
	v_pk_mul_f32 v[156:157], v[120:121], v[60:61]
	v_pk_fma_f32 v[154:155], v[104:105], v[4:5], v[154:155]
	v_pk_fma_f32 v[156:157], v[112:113], v[12:13], v[156:157]
	v_pk_fma_f32 v[148:149], v[108:109], v[16:17], v[148:149]
	v_pk_fma_f32 v[146:147], v[100:101], v[8:9], v[146:147]
	v_pk_fma_f32 v[144:145], v[110:111], v[10:11], v[144:145]
	v_pk_fma_f32 v[142:143], v[102:103], v[2:3], v[142:143]
	v_pk_fma_f32 v[140:141], v[106:107], v[14:15], v[140:141]
	v_pk_fma_f32 v[138:139], v[98:99], v[6:7], v[138:139]
	v_pk_add_f32 v[130:131], v[132:133], v[130:131]
	v_pk_add_f32 v[138:139], v[138:139], v[140:141]
	v_pk_add_f32 v[140:141], v[142:143], v[144:145]
	v_pk_add_f32 v[142:143], v[146:147], v[148:149]
	v_pk_add_f32 v[144:145], v[154:155], v[156:157]
	v_pk_add_f32 v[132:133], v[130:131], v[130:131] op_sel:[0,1] op_sel_hi:[1,0]
	v_pk_add_f32 v[142:143], v[144:145], v[142:143]
	v_pk_add_f32 v[138:139], v[140:141], v[138:139]
	v_add_f32_e32 v133, v142, v143
	v_add_f32_e32 v130, v138, v139
	s_waitcnt lgkmcnt(2)
	v_pk_mul_f32 v[138:139], v[90:91], v[54:55]
	s_waitcnt lgkmcnt(0)
	v_pk_mul_f32 v[140:141], v[94:95], v[62:63]
	v_pk_mul_f32 v[142:143], v[82:83], v[50:51]
	v_pk_mul_f32 v[144:145], v[86:87], v[58:59]
	v_pk_mul_f32 v[146:147], v[92:93], v[56:57]
	v_pk_mul_f32 v[148:149], v[96:97], v[64:65]
	v_pk_mul_f32 v[154:155], v[84:85], v[52:53]
	v_pk_mul_f32 v[156:157], v[88:89], v[60:61]
	v_add_f32_e32 v130, v130, v133
	v_pk_fma_f32 v[156:157], v[80:81], v[12:13], v[156:157]
	v_pk_fma_f32 v[154:155], v[72:73], v[4:5], v[154:155]
	v_pk_fma_f32 v[148:149], v[76:77], v[16:17], v[148:149]
	v_pk_fma_f32 v[146:147], v[68:69], v[8:9], v[146:147]
	v_pk_fma_f32 v[144:145], v[78:79], v[10:11], v[144:145]
	v_pk_fma_f32 v[142:143], v[70:71], v[2:3], v[142:143]
	v_pk_fma_f32 v[140:141], v[74:75], v[14:15], v[140:141]
	v_pk_fma_f32 v[138:139], v[66:67], v[6:7], v[138:139]
	v_mov_b32_e32 v133, v130
	v_pk_add_f32 v[138:139], v[138:139], v[140:141]
	v_pk_add_f32 v[140:141], v[142:143], v[144:145]
	v_pk_add_f32 v[142:143], v[146:147], v[148:149]
	v_pk_add_f32 v[144:145], v[154:155], v[156:157]
	v_permlane32_swap_b32_e32 v130, v133
	v_pk_add_f32 v[142:143], v[144:145], v[142:143]
	v_add_f32_e32 v160, v130, v133
	v_pk_add_f32 v[138:139], v[140:141], v[138:139]
	v_add_f32_e32 v133, v142, v143
	v_pk_add_f32 v[140:141], v[26:27], v[42:43]
	v_pk_add_f32 v[142:143], v[28:29], v[44:45]
	v_pk_add_f32 v[144:145], v[20:21], v[36:37]
	v_pk_add_f32 v[146:147], v[32:33], v[48:49]
	v_pk_add_f32 v[148:149], v[24:25], v[40:41]
	v_pk_add_f32 v[154:155], v[30:31], v[46:47]
	v_pk_add_f32 v[156:157], v[22:23], v[38:39]
	v_pk_add_f32 v[158:159], v[18:19], v[34:35]
	v_pk_add_f32 v[154:155], v[156:157], v[154:155]
	v_pk_add_f32 v[146:147], v[148:149], v[146:147]
	v_pk_add_f32 v[142:143], v[144:145], v[142:143]
	v_pk_add_f32 v[140:141], v[158:159], v[140:141]
	v_pk_add_f32 v[142:143], v[142:143], v[146:147]
	v_pk_add_f32 v[140:141], v[140:141], v[154:155]
	v_add_f32_e32 v130, v138, v139
	v_pk_mov_b32 v[144:145], v[140:141], v[142:143] op_sel:[1,0]
	v_mov_b32_e32 v141, v143
	v_pk_add_f32 v[140:141], v[144:145], v[140:141]
	v_add_f32_e32 v133, v130, v133
	v_pk_add_f32 v[140:141], v[140:141], v[140:141] op_sel:[0,1] op_sel_hi:[1,0]
	v_mov_b32_e32 v131, v132
	v_mov_b32_e32 v130, v140
	s_nop 1
	v_permlane32_swap_b32_e32 v140, v130
	v_add_f32_e32 v130, v140, v130
	v_fmamk_f32 v49, v130, 0xbc800000, v49
	v_fmamk_f32 v48, v130, 0xbc800000, v48
	v_fmamk_f32 v47, v130, 0xbc800000, v47
	v_fmamk_f32 v46, v130, 0xbc800000, v46
	v_fmamk_f32 v45, v130, 0xbc800000, v45
	v_fmamk_f32 v44, v130, 0xbc800000, v44
	v_fmamk_f32 v43, v130, 0xbc800000, v43
	v_fmamk_f32 v42, v130, 0xbc800000, v42
	v_fmamk_f32 v41, v130, 0xbc800000, v41
	v_fmamk_f32 v40, v130, 0xbc800000, v40
	v_fmamk_f32 v39, v130, 0xbc800000, v39
	v_fmamk_f32 v38, v130, 0xbc800000, v38
	v_fmamk_f32 v37, v130, 0xbc800000, v37
	v_fmamk_f32 v36, v130, 0xbc800000, v36
	v_fmamk_f32 v35, v130, 0xbc800000, v35
	v_fmac_f32_e32 v34, 0xbc800000, v130
	v_fmamk_f32 v33, v130, 0xbc800000, v33
	v_fmamk_f32 v32, v130, 0xbc800000, v32
	v_fmamk_f32 v31, v130, 0xbc800000, v31
	v_fmamk_f32 v30, v130, 0xbc800000, v30
	v_fmamk_f32 v29, v130, 0xbc800000, v29
	v_fmamk_f32 v28, v130, 0xbc800000, v28
	v_fmamk_f32 v27, v130, 0xbc800000, v27
	v_fmamk_f32 v26, v130, 0xbc800000, v26
	v_fmamk_f32 v25, v130, 0xbc800000, v25
	v_fmamk_f32 v24, v130, 0xbc800000, v24
	v_fmamk_f32 v23, v130, 0xbc800000, v23
	v_fmamk_f32 v22, v130, 0xbc800000, v22
	v_fmamk_f32 v21, v130, 0xbc800000, v21
	v_fmamk_f32 v20, v130, 0xbc800000, v20
	v_fmamk_f32 v19, v130, 0xbc800000, v19
	v_fmac_f32_e32 v18, 0xbc800000, v130
	v_pk_mul_f32 v[140:141], v[38:39], v[38:39]
	v_pk_mul_f32 v[142:143], v[46:47], v[46:47]
	v_pk_mul_f32 v[144:145], v[34:35], v[34:35]
	v_pk_mul_f32 v[146:147], v[42:43], v[42:43]
	v_pk_mul_f32 v[148:149], v[40:41], v[40:41]
	v_pk_mul_f32 v[154:155], v[48:49], v[48:49]
	v_pk_mul_f32 v[156:157], v[36:37], v[36:37]
	v_pk_mul_f32 v[158:159], v[44:45], v[44:45]
	v_pk_fma_f32 v[156:157], v[20:21], v[20:21], v[156:157]
	v_pk_fma_f32 v[158:159], v[28:29], v[28:29], v[158:159]
	v_pk_fma_f32 v[154:155], v[32:33], v[32:33], v[154:155]
	v_pk_fma_f32 v[148:149], v[24:25], v[24:25], v[148:149]
	v_pk_fma_f32 v[146:147], v[26:27], v[26:27], v[146:147]
	v_pk_fma_f32 v[144:145], v[18:19], v[18:19], v[144:145]
	v_pk_fma_f32 v[142:143], v[30:31], v[30:31], v[142:143]
	v_pk_fma_f32 v[140:141], v[22:23], v[22:23], v[140:141]
	v_permlane32_swap_b32_e32 v132, v131
	v_pk_add_f32 v[140:141], v[140:141], v[142:143]
	v_pk_add_f32 v[142:143], v[144:145], v[146:147]
	v_pk_add_f32 v[144:145], v[148:149], v[154:155]
	v_pk_add_f32 v[146:147], v[156:157], v[158:159]
	v_pk_add_f32 v[140:141], v[142:143], v[140:141]
	v_pk_add_f32 v[144:145], v[146:147], v[144:145]
	v_pk_mul_f32 v[122:123], v[122:123], v[38:39]
	v_pk_mov_b32 v[142:143], v[140:141], v[144:145] op_sel:[1,0]
	v_mov_b32_e32 v141, v145
	v_pk_add_f32 v[140:141], v[142:143], v[140:141]
	v_pk_mul_f32 v[126:127], v[126:127], v[46:47]
	v_pk_add_f32 v[140:141], v[140:141], v[140:141] op_sel:[0,1] op_sel_hi:[1,0]
	v_pk_mul_f32 v[114:115], v[114:115], v[34:35]
	v_mov_b32_e32 v130, v140
	s_nop 1
	v_permlane32_swap_b32_e32 v140, v130
	v_mov_b32_e32 v141, v132
	v_pk_add_f32 v[130:131], v[140:141], v[130:131]
	v_pk_mul_f32 v[118:119], v[118:119], v[42:43]
	v_pk_fma_f32 v[130:131], v[130:131], s[0:1], v[152:153] op_sel_hi:[1,0,0]
	v_pk_mul_f32 v[124:125], v[124:125], v[40:41]
	v_mul_f32_e32 v132, 0x4b800000, v131
	v_cmp_gt_f32_e32 vcc, s1, v131
	v_pk_mul_f32 v[128:129], v[128:129], v[48:49]
	v_pk_mul_f32 v[116:117], v[116:117], v[36:37]
	v_pk_mul_f32 v[120:121], v[120:121], v[44:45]
	v_cndmask_b32_e32 v131, v131, v132, vcc
	v_mul_f32_e32 v132, 0x4b800000, v130
	v_cmp_gt_f32_e64 s[0:1], s1, v130
	v_pk_fma_f32 v[112:113], v[112:113], v[28:29], v[120:121]
	v_pk_fma_f32 v[104:105], v[104:105], v[20:21], v[116:117]
	v_pk_fma_f32 v[108:109], v[108:109], v[32:33], v[128:129]
	v_pk_fma_f32 v[100:101], v[100:101], v[24:25], v[124:125]
	v_pk_fma_f32 v[110:111], v[110:111], v[26:27], v[118:119]
	v_pk_fma_f32 v[102:103], v[102:103], v[18:19], v[114:115]
	v_pk_fma_f32 v[106:107], v[106:107], v[30:31], v[126:127]
	v_pk_fma_f32 v[98:99], v[98:99], v[22:23], v[122:123]
	v_rsq_f32_e32 v131, v131
	v_cndmask_b32_e64 v130, v130, v132, s[0:1]
	v_pk_add_f32 v[98:99], v[98:99], v[106:107]
	v_pk_add_f32 v[102:103], v[102:103], v[110:111]
	v_pk_add_f32 v[100:101], v[100:101], v[108:109]
	v_pk_add_f32 v[104:105], v[104:105], v[112:113]
	v_rsq_f32_e32 v132, v130
	v_pk_add_f32 v[100:101], v[104:105], v[100:101]
	v_pk_add_f32 v[98:99], v[102:103], v[98:99]
	v_mul_f32_e32 v130, 0x45800000, v131
	v_add_f32_e32 v98, v98, v99
	v_add_f32_e32 v99, v100, v101
	v_add_f32_e32 v98, v98, v99
	v_mov_b32_e32 v99, v98
	v_pk_mul_f32 v[90:91], v[90:91], v[38:39]
	v_pk_mul_f32 v[94:95], v[94:95], v[46:47]
	v_pk_mul_f32 v[82:83], v[82:83], v[34:35]
	v_pk_mul_f32 v[86:87], v[86:87], v[42:43]
	v_cndmask_b32_e32 v130, v131, v130, vcc
	v_mul_f32_e32 v131, 0x45800000, v132
	v_permlane32_swap_b32_e32 v98, v99
	v_pk_fma_f32 v[78:79], v[78:79], v[26:27], v[86:87]
	v_pk_fma_f32 v[70:71], v[70:71], v[18:19], v[82:83]
	v_pk_fma_f32 v[74:75], v[74:75], v[30:31], v[94:95]
	v_pk_fma_f32 v[66:67], v[66:67], v[22:23], v[90:91]
	v_cndmask_b32_e64 v131, v132, v131, s[0:1]
	v_add_f32_e32 v98, v98, v99
	v_pk_add_f32 v[66:67], v[66:67], v[74:75]
	v_pk_add_f32 v[70:71], v[70:71], v[78:79]
	v_mul_f32_e32 v139, v160, v130
	v_mul_f32_e32 v98, v98, v131
	v_pk_add_f32 v[66:67], v[70:71], v[66:67]
	v_cmp_gt_u32_e32 vcc, 32, v1
	v_add_f32_e32 v66, v66, v67
	v_pk_mul_f32 v[92:93], v[92:93], v[40:41]
	v_cndmask_b32_e32 v67, v98, v139, vcc
	v_add_f32_e32 v67, s12, v67
	v_pk_mul_f32 v[96:97], v[96:97], v[48:49]
	v_pk_mul_f32 v[84:85], v[84:85], v[36:37]
	v_pk_mul_f32 v[88:89], v[88:89], v[44:45]
	v_mul_f32_e32 v67, 0xbfb8aa3b, v67
	v_pk_fma_f32 v[80:81], v[80:81], v[28:29], v[88:89]
	v_pk_fma_f32 v[72:73], v[72:73], v[20:21], v[84:85]
	v_pk_fma_f32 v[76:77], v[76:77], v[32:33], v[96:97]
	v_pk_fma_f32 v[68:69], v[68:69], v[24:25], v[92:93]
	v_exp_f32_e32 v70, v67
	v_pk_add_f32 v[68:69], v[68:69], v[76:77]
	v_pk_add_f32 v[72:73], v[72:73], v[80:81]
	v_cmp_lt_i32_e64 s[0:1], 0, v151
	v_pk_add_f32 v[68:69], v[72:73], v[68:69]
	v_mov_b32_e32 v137, v136
	v_add_f32_e32 v67, v68, v69
	v_add_f32_e32 v67, v66, v67
	v_add_f32_e32 v66, 1.0, v70
	v_rcp_f32_e32 v66, v66
	v_mov_b32_e32 v69, 0xff800000
	v_mov_b32_e32 v138, v133
	v_mov_b32_e32 v68, v67
	v_cndmask_b32_e64 v70, v69, v66, s[0:1]
	v_mbcnt_lo_u32_b32 v66, -1, 0
	v_mbcnt_hi_u32_b32 v66, -1, v66
	v_permlane32_swap_b32_e32 v136, v137
	v_permlane32_swap_b32_e32 v133, v138
	v_permlane32_swap_b32_e32 v67, v68
	v_and_b32_e32 v86, 64, v66
	s_mov_b32 s14, 8
	s_mov_b32 s13, 0
	v_mov_b32_e32 v66, 0
	s_waitcnt lgkmcnt(0)
